# speedup vs baseline: 1.0065x; 1.0027x over previous
.Lst3_join:
	v_mfma_scale_f32_16x16x128_f8f6f4 v[80:83], v[46:51], v[40:45], v[80:83], v187, v187 op_sel_hi:[0,0,0] cbsz:2 blgp:2
	v_mfma_scale_f32_16x16x128_f8f6f4 v[72:75], v[194:199], v[40:45], v[72:75], v187, v187 op_sel_hi:[0,0,0] cbsz:2 blgp:2
	v_mfma_scale_f32_16x16x128_f8f6f4 v[64:67], v[200:205], v[40:45], v[64:67], v187, v187 op_sel_hi:[0,0,0] cbsz:2 blgp:2
	v_mfma_scale_f32_16x16x128_f8f6f4 v[56:59], v[206:211], v[40:45], v[56:59], v187, v187 op_sel_hi:[0,0,0] cbsz:2 blgp:2
	v_mfma_scale_f32_16x16x128_f8f6f4 v[52:55], v[46:51], v[188:193], v[52:55], v187, v187 op_sel_hi:[0,0,0] cbsz:2 blgp:2
	v_mfma_scale_f32_16x16x128_f8f6f4 v[48:51], v[194:199], v[188:193], v[224:227], v187, v187 op_sel_hi:[0,0,0] cbsz:2 blgp:2
	v_mfma_scale_f32_16x16x128_f8f6f4 v[44:47], v[200:205], v[188:193], v[212:215], v187, v187 op_sel_hi:[0,0,0] cbsz:2 blgp:2
	v_mfma_scale_f32_16x16x128_f8f6f4 v[40:43], v[206:211], v[188:193], v[216:219], v187, v187 op_sel_hi:[0,0,0] cbsz:2 blgp:2
	s_add_i32 s36, s36, 2
	s_add_u32 s11, s11, 0xc000
	s_addc_u32 s35, s35, 0
	s_add_u32 s2, s2, 0xc000
	s_addc_u32 s3, s3, 0
	s_add_u32 s72, s72, 0xc000
	s_addc_u32 s73, s73, 0
	s_cmp_lt_u32 s36, 4
	s_waitcnt lgkmcnt(0)
	s_cbranch_scc1 .LBB1_3
.LBB1_5:
	ds_read_b128 v[188:191], v1 offset:24576
	ds_read_b64 v[192:193], v172 offset:24640
	ds_read_b128 v[194:197], v1 offset:26112
	ds_read_b64 v[198:199], v172 offset:26176
	ds_read_b128 v[200:203], v170 offset:36864
	ds_read_b64 v[204:205], v173 offset:36928
	ds_read_b128 v[206:209], v170 offset:38400
	ds_read_b64 v[210:211], v173 offset:38464
	ds_read_b128 v[212:215], v170 offset:39936
	ds_read_b64 v[216:217], v173 offset:40000
	ds_read_b128 v[218:221], v170 offset:41472
	ds_read_b64 v[222:223], v173 offset:41536
	v_mfma_scale_f32_16x16x128_f8f6f4 v[164:167], v[2:7], v[20:25], v[164:167], v187, v187 op_sel_hi:[0,0,0] cbsz:2 blgp:2
	v_mfma_scale_f32_16x16x128_f8f6f4 v[160:163], v[8:13], v[20:25], v[160:163], v187, v187 op_sel_hi:[0,0,0] cbsz:2 blgp:2
	v_mfma_scale_f32_16x16x128_f8f6f4 v[156:159], v[14:19], v[20:25], v[156:159], v187, v187 op_sel_hi:[0,0,0] cbsz:2 blgp:2
	v_mfma_scale_f32_16x16x128_f8f6f4 v[152:155], v[26:31], v[20:25], v[152:155], v187, v187 op_sel_hi:[0,0,0] cbsz:2 blgp:2
	v_mfma_scale_f32_16x16x128_f8f6f4 v[148:151], v[2:7], v[32:37], v[148:151], v187, v187 op_sel_hi:[0,0,0] cbsz:2 blgp:2
	v_mfma_scale_f32_16x16x128_f8f6f4 v[140:143], v[8:13], v[32:37], v[140:143], v187, v187 op_sel_hi:[0,0,0] cbsz:2 blgp:2
	v_mfma_scale_f32_16x16x128_f8f6f4 v[132:135], v[14:19], v[32:37], v[132:135], v187, v187 op_sel_hi:[0,0,0] cbsz:2 blgp:2
	v_mfma_scale_f32_16x16x128_f8f6f4 v[124:127], v[26:31], v[32:37], v[124:127], v187, v187 op_sel_hi:[0,0,0] cbsz:2 blgp:2
	s_cbranch_vccz .Ltail_nowait
	s_waitcnt vmcnt(0)
